# PEER expert phase: the two hand-written inner loop heads padded to 64-byte boundaries (s_nop padding before the loops)
# baseline (speedup 1.0000x reference)
; #define LAS __attribute__((address_space(3)))
; #define LDS_WAIT() asm volatile("s_waitcnt lgkmcnt(0)" ::: "memory")
; __device__ __forceinline__ void expert_phase(const Frame& F, int l, int xcc, LAS unsigned char* wl, const LAS unsigned char* zb) {
;     ...
;             const LAS unsigned char* bbase = c < 2 ? BI + c * 128 + rq * 32 : zb;
;             LAS unsigned char* bw = BI + (lane >> 5) * 256 + (((lane & 31) >> 2) & 3) * 32 + ((lane & 31) >> 4) * 16 + (lane & 3) * 4;
;             auto u_x = [&](int i) { return ldo_u2(X1 + (size_t)tok(i & 7) * D + slice_of(i) * 256, 8u * lane); };
;             struct HRows { u32x4 r[8]; };
;             auto u_rows_h = [&](int hs, HRows& H) {
;                 const int i = hs >> 1, mg = hs & 1;
;                 const unsigned char* Usl = UBl + (size_t)slice_of(i) * XSL_BYTES;
;                 const u32x2 id = *(const LAS u32x2*)(IDL + (i & 7) * 256 + c * 16 + mg * 8);
;     ...
;                 const unsigned pm = (U_REP > 1 && urep == 0) ? (unsigned)(U_PROBE_MASK) : 0xffffu;
;     ...
;                 const unsigned pm = 0xffffu;
;     ...
;                 const unsigned i0 = id.x, i1 = id.y;
; #pragma unroll
;                 for (int mm = 0; mm < 4; ++mm) { const unsigned w = mm < 2 ? i0 : i1; const unsigned e = (mm & 1) ? (w >> 16) : (w & 0xffffu); const unsigned off = (e & pm) * 128u + 16u * rq;
;                     H.r[2 * mm] = ldo_u4(Usl, off); H.r[2 * mm + 1] = ldo_u4(Usl + 64, off); }
;             };
;             i32x8 B0, B1;
;             auto u_bbuild = [&](int i, const u32x2& xw) {
;                 const int k = i & 7;
;                 const f32x4 gg = *(const LAS f32x4*)(G2 + slice_of(i) * 256 + 4 * lane);
;                 const float rstd = RS[k];
;                 const float h0 = bf_lo(xw.x) * rstd * gg[0], h1 = bf_hi(xw.x) * rstd * gg[1], h2 = bf_lo(xw.y) * rstd * gg[2], h3 = bf_hi(xw.y) * rstd * gg[3];
;                 int w = __builtin_amdgcn_cvt_pk_fp8_f32(h0, h1, 0, false); w = __builtin_amdgcn_cvt_pk_fp8_f32(h2, h3, w, true);
;                 const f32x2 b0 = __builtin_amdgcn_cvt_pk_f32_fp8(w, false), b1 = __builtin_amdgcn_cvt_pk_f32_fp8(w, true);
;                 int v = __builtin_amdgcn_cvt_pk_fp8_f32(h0 - b0[0], h1 - b0[1], 0, false); v = __builtin_amdgcn_cvt_pk_fp8_f32(h2 - b1[0], h3 - b1[1], v, true);
;                 *(LAS int*)(bw) = w; *(LAS int*)(bw + 128) = v;
;                 LDS_WAIT(); XFENCE();
.LBB0_1141:
	s_or_b64 exec, exec, s[64:65]
	s_waitcnt lgkmcnt(0)
	s_mov_b32 s100, 0xcccccccc
	s_mov_b32 s101, 0xcccccccc
	s_movk_i32 s5, 0x80
	v_and_b32_e32 v128, 15, v211
	v_lshrrev_b32_e32 v129, 4, v211
	v_lshrrev_b32_e32 v130, 2, v128
	v_lshrrev_b32_e32 v131, 1, v129
	v_lshl_add_u32 v130, v130, 1, v131
	v_lshlrev_b32_e32 v240, 5, v130
	v_add_u32_e32 v240, s83, v240
	v_add_u32_e32 v240, 0x2a40, v240
	v_and_b32_e32 v130, 3, v128
	v_and_b32_e32 v132, 1, v129
	v_lshl_add_u32 v133, v132, 2, v130
	v_lshlrev_b32_e32 v241, 4, v133
	v_and_b32_e32 v133, 1, v130
	v_lshl_add_u32 v133, v133, 1, v132
	v_lshlrev_b32_e32 v133, 5, v133
	v_lshl_add_u32 v133, v131, 8, v133
	v_lshrrev_b32_e32 v134, 3, v128
	v_lshl_add_u32 v133, v134, 7, v133
	v_lshrrev_b32_e32 v135, 1, v130
	v_lshl_add_u32 v133, v135, 4, v133
	v_add_u32_e32 v133, s83, v133
	v_add_u32_e32 v133, 0x2840, v133
	v_bfe_u32 v135, v128, 2, 1
	v_cmp_eq_u32_e32 vcc, 0, v135
	v_mov_b32_e32 v131, 0x1a000
	s_nop 1
	v_cndmask_b32_e32 v242, v131, v133, vcc
	v_cndmask_b32_e32 v249, v133, v131, vcc
	v_lshl_add_u32 v133, v129, 1, v135
	v_lshlrev_b32_e32 v133, 3, v133
	v_lshl_add_u32 v133, v134, 6, v133
	v_lshl_add_u32 v133, v130, 7, v133
	v_add_u32_e32 v243, s83, v133
	s_mov_b32 vcc_lo, 0xaaaaaaaa
	s_mov_b32 vcc_hi, 0xaaaaaaaa
	s_mov_b32 s77, -2
	s_add_i32 s33, s77, 2
	s_min_i32 s33, s33, 63
	s_lshr_b32 s58, s33, 3
	s_add_i32 s58, s58, s96
	s_and_b32 s58, s58, 7
	s_and_b32 s33, s33, 7
	s_lshl_b32 s78, s58, 21
	s_add_u32 s64, s53, s78
	s_addc_u32 s65, s56, 0
	s_mul_i32 s78, s33, s82
	s_add_i32 s78, s78, s26
	s_cmpk_lt_i32 s78, 0x4000
	s_cselect_b32 s78, s78, s26
	s_ashr_i32 s55, s78, 31
	s_mov_b32 s54, s78
	s_lshl_b64 s[54:55], s[54:55], 12
	s_add_u32 s54, s90, s54
	s_addc_u32 s55, s91, s55
	s_lshl_b32 s78, s58, 9
	s_add_u32 s54, s54, s78
	s_addc_u32 s55, s55, 0
	v_lshl_add_u64 v[208:209], s[54:55], 0, v[184:185]
	global_load_dwordx2 v[172:173], v[208:209], off
	s_lshl_b32 s78, s33, 8
	v_add_u32_e32 v248, s78, v240
	ds_read_b128 v[236:239], v248 offset:0
	s_waitcnt lgkmcnt(0)
	v_mad_u32_u16 v208, v236, s5, v241 op_sel:[0,0,0,0]
	global_load_dwordx4 v[0:3], v208, s[64:65]
	v_mad_u32_u16 v209, v236, s5, v241 op_sel:[1,0,0,0]
	global_load_dwordx4 v[4:7], v209, s[64:65]
	v_mad_u32_u16 v208, v237, s5, v241 op_sel:[0,0,0,0]
	global_load_dwordx4 v[8:11], v208, s[64:65]
	v_mad_u32_u16 v209, v237, s5, v241 op_sel:[1,0,0,0]
	global_load_dwordx4 v[12:15], v209, s[64:65]
	v_mad_u32_u16 v208, v238, s5, v241 op_sel:[0,0,0,0]
	global_load_dwordx4 v[16:19], v208, s[64:65]
	v_mad_u32_u16 v209, v238, s5, v241 op_sel:[1,0,0,0]
	global_load_dwordx4 v[20:23], v209, s[64:65]
	v_mad_u32_u16 v208, v239, s5, v241 op_sel:[0,0,0,0]
	global_load_dwordx4 v[24:27], v208, s[64:65]
	v_mad_u32_u16 v209, v239, s5, v241 op_sel:[1,0,0,0]
	global_load_dwordx4 v[28:31], v209, s[64:65]
	s_lshl_b32 s78, s33, 8
	v_add_u32_e32 v248, s78, v240
	ds_read_b128 v[236:239], v248 offset:16
	s_waitcnt lgkmcnt(0)
	v_mad_u32_u16 v208, v236, s5, v241 op_sel:[0,0,0,0]
	global_load_dwordx4 v[32:35], v208, s[64:65]
	v_mad_u32_u16 v209, v236, s5, v241 op_sel:[1,0,0,0]
	global_load_dwordx4 v[36:39], v209, s[64:65]
	v_mad_u32_u16 v208, v237, s5, v241 op_sel:[0,0,0,0]
	global_load_dwordx4 v[40:43], v208, s[64:65]
	v_mad_u32_u16 v209, v237, s5, v241 op_sel:[1,0,0,0]
	global_load_dwordx4 v[44:47], v209, s[64:65]
	v_mad_u32_u16 v208, v238, s5, v241 op_sel:[0,0,0,0]
	global_load_dwordx4 v[48:51], v208, s[64:65]
	v_mad_u32_u16 v209, v238, s5, v241 op_sel:[1,0,0,0]
	global_load_dwordx4 v[52:55], v209, s[64:65]
	v_mad_u32_u16 v208, v239, s5, v241 op_sel:[0,0,0,0]
	global_load_dwordx4 v[56:59], v208, s[64:65]
	v_mad_u32_u16 v209, v239, s5, v241 op_sel:[1,0,0,0]
	global_load_dwordx4 v[60:63], v209, s[64:65]
	s_mov_b32 s77, -1
	s_add_i32 s33, s77, 2
	s_min_i32 s33, s33, 63
	s_lshr_b32 s58, s33, 3
	s_add_i32 s58, s58, s96
	s_and_b32 s58, s58, 7
	s_and_b32 s33, s33, 7
	s_lshl_b32 s78, s58, 21
	s_add_u32 s64, s53, s78
	s_addc_u32 s65, s56, 0
	s_mul_i32 s78, s33, s82
	s_add_i32 s78, s78, s26
	s_cmpk_lt_i32 s78, 0x4000
	s_cselect_b32 s78, s78, s26
	s_ashr_i32 s55, s78, 31
	s_mov_b32 s54, s78
	s_lshl_b64 s[54:55], s[54:55], 12
	s_add_u32 s54, s90, s54
	s_addc_u32 s55, s91, s55
	s_lshl_b32 s78, s58, 9
	s_add_u32 s54, s54, s78
	s_addc_u32 s55, s55, 0
	v_lshl_add_u64 v[208:209], s[54:55], 0, v[184:185]
	global_load_dwordx2 v[174:175], v[208:209], off
	s_lshl_b32 s78, s33, 8
	v_add_u32_e32 v248, s78, v240
	ds_read_b128 v[236:239], v248 offset:0
	s_waitcnt lgkmcnt(0)
	v_mad_u32_u16 v208, v236, s5, v241 op_sel:[0,0,0,0]
	global_load_dwordx4 v[64:67], v208, s[64:65]
	v_mad_u32_u16 v209, v236, s5, v241 op_sel:[1,0,0,0]
	global_load_dwordx4 v[68:71], v209, s[64:65]
	v_mad_u32_u16 v208, v237, s5, v241 op_sel:[0,0,0,0]
	global_load_dwordx4 v[72:75], v208, s[64:65]
	v_mad_u32_u16 v209, v237, s5, v241 op_sel:[1,0,0,0]
	global_load_dwordx4 v[76:79], v209, s[64:65]
	v_mad_u32_u16 v208, v238, s5, v241 op_sel:[0,0,0,0]
	global_load_dwordx4 v[80:83], v208, s[64:65]
	v_mad_u32_u16 v209, v238, s5, v241 op_sel:[1,0,0,0]
	global_load_dwordx4 v[84:87], v209, s[64:65]
	v_mad_u32_u16 v208, v239, s5, v241 op_sel:[0,0,0,0]
	global_load_dwordx4 v[88:91], v208, s[64:65]
	v_mad_u32_u16 v209, v239, s5, v241 op_sel:[1,0,0,0]
	global_load_dwordx4 v[92:95], v209, s[64:65]
	s_lshl_b32 s78, s33, 8
	v_add_u32_e32 v248, s78, v240
	ds_read_b128 v[236:239], v248 offset:16
	s_waitcnt lgkmcnt(0)
	v_mad_u32_u16 v208, v236, s5, v241 op_sel:[0,0,0,0]
	global_load_dwordx4 v[96:99], v208, s[64:65]
	v_mad_u32_u16 v209, v236, s5, v241 op_sel:[1,0,0,0]
	global_load_dwordx4 v[100:103], v209, s[64:65]
	v_mad_u32_u16 v208, v237, s5, v241 op_sel:[0,0,0,0]
	global_load_dwordx4 v[104:107], v208, s[64:65]
	v_mad_u32_u16 v209, v237, s5, v241 op_sel:[1,0,0,0]
	global_load_dwordx4 v[108:111], v209, s[64:65]
	v_mad_u32_u16 v208, v238, s5, v241 op_sel:[0,0,0,0]
	global_load_dwordx4 v[112:115], v208, s[64:65]
	v_mad_u32_u16 v209, v238, s5, v241 op_sel:[1,0,0,0]
	global_load_dwordx4 v[116:119], v209, s[64:65]
	v_mad_u32_u16 v208, v239, s5, v241 op_sel:[0,0,0,0]
	global_load_dwordx4 v[120:123], v208, s[64:65]
	v_mad_u32_u16 v209, v239, s5, v241 op_sel:[1,0,0,0]
	global_load_dwordx4 v[124:127], v209, s[64:65]
	s_mov_b32 s77, 0
	s_nop 0
	s_nop 0
	s_nop 0
	s_nop 0
	s_nop 0
	s_nop 0
	s_nop 0
	s_nop 0
	s_nop 0
	s_nop 0
	s_nop 0
	s_nop 0
	s_nop 0

; #define LAS __attribute__((address_space(3)))
; __device__ __forceinline__ void expert_phase(const Frame& F, int l, int xcc, LAS unsigned char* wl, const LAS unsigned char* zb) {
;     ...
;                 const LAS u32x4* wp = (const LAS u32x4*)(SA + k * 256 + 16 * rr);
;                 const u32x4 wall[4] = {wp[0], wp[1], wp[2], wp[3]};
;                 unsigned out[16];
; #pragma unroll
;                 for (int j = 0; j < 16; ++j) out[j] = 0u;
; #pragma unroll
;                 for (int j = 0; j < 16; ++j) {
;                     if (j == 8) xw = ldo_u2(X1 + (size_t)t * D + sl * 256, 2u * col);
;                     u32x4 rj = R.r[j];
;                     asm volatile("" : "+v"(rj.x), "+v"(rj.y), "+v"(rj.z), "+v"(rj.w) :: "memory");
;                     const unsigned wj = wall[j >> 2][j & 3]; const hf2 w2 = __builtin_bit_cast(hf2, wj);
; #pragma unroll
;                     for (int d = 0; d < 4; ++d) {
;                         const hf2 a = __builtin_amdgcn_cvt_scalef32_pk_f16_fp4(rj[d], 1.0f, 0), b = __builtin_amdgcn_cvt_scalef32_pk_f16_fp4(rj[d], 1.0f, 1),
;                                   cc = __builtin_amdgcn_cvt_scalef32_pk_f16_fp4(rj[d], 1.0f, 2), dd = __builtin_amdgcn_cvt_scalef32_pk_f16_fp4(rj[d], 1.0f, 3);
;                         out[4 * d] = __builtin_bit_cast(unsigned, __builtin_elementwise_fma(a, w2, __builtin_bit_cast(hf2, out[4 * d])));
;                         out[4 * d + 1] = __builtin_bit_cast(unsigned, __builtin_elementwise_fma(b, w2, __builtin_bit_cast(hf2, out[4 * d + 1])));
;                         out[4 * d + 2] = __builtin_bit_cast(unsigned, __builtin_elementwise_fma(cc, w2, __builtin_bit_cast(hf2, out[4 * d + 2])));
;                         out[4 * d + 3] = __builtin_bit_cast(unsigned, __builtin_elementwise_fma(dd, w2, __builtin_bit_cast(hf2, out[4 * d + 3])));
.LBB0_1239:
	s_or_b64 exec, exec, s[2:3]
	s_waitcnt vmcnt(0) lgkmcnt(0)
	v_and_b32_e32 v120, 7, v211
	v_lshrrev_b32_e32 v121, 3, v211
	v_and_b32_e32 v122, 15, v211
	v_lshrrev_b32_e32 v123, 4, v211
	s_lshr_b32 s2, s83, 10
	s_mul_i32 s2, s2, 79
	s_lshr_b32 s2, s2, 10
	s_mul_i32 s3, s2, 0x1200
	s_mov_b32 s8, 0x1c200
	s_mov_b32 s9, 0x1cc00
	s_cmp_lt_u32 s2, 3
	s_cselect_b32 s8, s8, s9
	s_mov_b32 s9, 0x1d400
	s_cmp_lt_u32 s2, 6
	s_cselect_b32 s8, s8, s9
	s_add_i32 s3, s3, s8
	v_lshlrev_b32_e32 v113, 4, v120
	v_mul_u32_u24_e32 v110, 0x240, v121
	v_add3_u32 v110, v110, v113, s3
	v_mul_u32_u24_e32 v111, 0x90, v122
	v_lshl_add_u32 v111, v123, 3, v111
	v_add_u32_e32 v111, s3, v111
	v_lshlrev_b32_e32 v112, 3, v121
	v_add_u32_e32 v112, s83, v112
	v_add_u32_e32 v112, 0x2a40, v112
	v_lshrrev_b32_e32 v124, 2, v122
	v_and_b32_e32 v125, 1, v123
	v_lshlrev_b32_e32 v114, 7, v124
	v_lshl_add_u32 v114, v125, 4, v114
	v_add_u32_e32 v114, s83, v114
	v_add_u32_e32 v114, 0x200, v114
	v_and_b32_e32 v126, 3, v211
	v_lshlrev_b32_e32 v115, 6, v126
	v_lshl_add_u32 v115, v123, 4, v115
	v_add_u32_e32 v115, s83, v115
	v_lshlrev_b32_e32 v116, 4, v122
	v_lshl_add_u32 v116, v123, 10, v116
	v_add_u32_e32 v116, s83, v116
	v_lshl_add_u32 v117, v211, 2, s83
	v_add_u32_e32 v117, 0x2000, v117
	v_lshl_add_u32 v118, v211, 2, s83
	v_add_u32_e32 v119, s83, v211
	v_add_u32_e32 v119, 0x200, v119
	s_mov_b32 s30, 0x1110111
	s_mov_b32 s31, 0x2220222
	s_mov_b32 s44, 0x4440444
	s_mov_b32 s45, 0x8880888
	s_mov_b32 s100, 0xf000f
	s_mov_b32 s101, 0xf000f
	s_mov_b32 s77, 0x7fff80
	s_mov_b32 s66, 0x07060302
	s_mov_b32 s68, 0x7fff
	ds_read2st64_b32 v[120:121], v118 offset0:0 offset1:1
	s_waitcnt lgkmcnt(0)
	v_cvt_f32_f16_e32 v122, v120
	v_cvt_f32_f16_e32 v123, v121
	v_cvt_pk_fp8_f32 v124, v122, v122
	v_cvt_pk_fp8_f32 v125, v123, v123
	s_nop 0
	ds_write_b8 v119, v124 offset:0
	ds_write_b8 v119, v125 offset:64
	v_cvt_f32_fp8_e32 v126, v124
	v_cvt_f32_fp8_e32 v127, v125
	s_nop 0
	v_sub_f32_e32 v128, v122, v126
	v_sub_f32_e32 v129, v123, v127
	v_cvt_pk_fp8_f32 v124, v128, v128
	v_cvt_pk_fp8_f32 v125, v129, v129
	s_nop 0
	ds_write_b8 v119, v124 offset:128
	ds_write_b8 v119, v125 offset:192
	v_cvt_f32_fp8_e32 v126, v124
	v_cvt_f32_fp8_e32 v127, v125
	s_nop 0
	v_sub_f32_e32 v128, v128, v126
	v_sub_f32_e32 v129, v129, v127
	v_cvt_pk_fp8_f32 v124, v128, v128
	v_cvt_pk_fp8_f32 v125, v129, v129
	s_nop 0
	ds_write_b8 v119, v124 offset:256
	ds_write_b8 v119, v125 offset:320
	ds_read2st64_b32 v[120:121], v118 offset0:4 offset1:5
	s_waitcnt lgkmcnt(0)
	v_cvt_f32_f16_e32 v122, v120
	v_cvt_f32_f16_e32 v123, v121
	v_cvt_pk_fp8_f32 v124, v122, v122
	v_cvt_pk_fp8_f32 v125, v123, v123
	s_nop 0
	ds_write_b8 v119, v124 offset:1024
	ds_write_b8 v119, v125 offset:1088
	v_cvt_f32_fp8_e32 v126, v124
	v_cvt_f32_fp8_e32 v127, v125
	s_nop 0
	v_sub_f32_e32 v128, v122, v126
	v_sub_f32_e32 v129, v123, v127
	v_cvt_pk_fp8_f32 v124, v128, v128
	v_cvt_pk_fp8_f32 v125, v129, v129
	s_nop 0
	ds_write_b8 v119, v124 offset:1152
	ds_write_b8 v119, v125 offset:1216
	v_cvt_f32_fp8_e32 v126, v124
	v_cvt_f32_fp8_e32 v127, v125
	s_nop 0
	v_sub_f32_e32 v128, v128, v126
	v_sub_f32_e32 v129, v129, v127
	v_cvt_pk_fp8_f32 v124, v128, v128
	v_cvt_pk_fp8_f32 v125, v129, v129
	s_nop 0
	ds_write_b8 v119, v124 offset:1280
	ds_write_b8 v119, v125 offset:1344
	ds_read2st64_b32 v[120:121], v118 offset0:8 offset1:9
	s_waitcnt lgkmcnt(0)
	v_cvt_f32_f16_e32 v122, v120
	v_cvt_f32_f16_e32 v123, v121
	v_cvt_pk_fp8_f32 v124, v122, v122
	v_cvt_pk_fp8_f32 v125, v123, v123
	s_nop 0
	ds_write_b8 v119, v124 offset:2048
	ds_write_b8 v119, v125 offset:2112
	v_cvt_f32_fp8_e32 v126, v124
	v_cvt_f32_fp8_e32 v127, v125
	s_nop 0
	v_sub_f32_e32 v128, v122, v126
	v_sub_f32_e32 v129, v123, v127
	v_cvt_pk_fp8_f32 v124, v128, v128
	v_cvt_pk_fp8_f32 v125, v129, v129
	s_nop 0
	ds_write_b8 v119, v124 offset:2176
	ds_write_b8 v119, v125 offset:2240
	v_cvt_f32_fp8_e32 v126, v124
	v_cvt_f32_fp8_e32 v127, v125
	s_nop 0
	v_sub_f32_e32 v128, v128, v126
	v_sub_f32_e32 v129, v129, v127
	v_cvt_pk_fp8_f32 v124, v128, v128
	v_cvt_pk_fp8_f32 v125, v129, v129
	s_nop 0
	ds_write_b8 v119, v124 offset:2304
	ds_write_b8 v119, v125 offset:2368
	ds_read2st64_b32 v[120:121], v118 offset0:12 offset1:13
	s_waitcnt lgkmcnt(0)
	v_cvt_f32_f16_e32 v122, v120
	v_cvt_f32_f16_e32 v123, v121
	v_cvt_pk_fp8_f32 v124, v122, v122
	v_cvt_pk_fp8_f32 v125, v123, v123
	s_nop 0
	ds_write_b8 v119, v124 offset:3072
	ds_write_b8 v119, v125 offset:3136
	v_cvt_f32_fp8_e32 v126, v124
	v_cvt_f32_fp8_e32 v127, v125
	s_nop 0
	v_sub_f32_e32 v128, v122, v126
	v_sub_f32_e32 v129, v123, v127
	v_cvt_pk_fp8_f32 v124, v128, v128
	v_cvt_pk_fp8_f32 v125, v129, v129
	s_nop 0
	ds_write_b8 v119, v124 offset:3200
	ds_write_b8 v119, v125 offset:3264
	v_cvt_f32_fp8_e32 v126, v124
	v_cvt_f32_fp8_e32 v127, v125
	s_nop 0
	v_sub_f32_e32 v128, v128, v126
	v_sub_f32_e32 v129, v129, v127
	v_cvt_pk_fp8_f32 v124, v128, v128
	v_cvt_pk_fp8_f32 v125, v129, v129
	s_nop 0
	ds_write_b8 v119, v124 offset:3328
	ds_write_b8 v119, v125 offset:3392
	ds_read2st64_b32 v[120:121], v118 offset0:16 offset1:17
	s_waitcnt lgkmcnt(0)
	v_cvt_f32_f16_e32 v122, v120
	v_cvt_f32_f16_e32 v123, v121
	v_cvt_pk_fp8_f32 v124, v122, v122
	v_cvt_pk_fp8_f32 v125, v123, v123
	s_nop 0
	ds_write_b8 v119, v124 offset:4096
	ds_write_b8 v119, v125 offset:4160
	v_cvt_f32_fp8_e32 v126, v124
	v_cvt_f32_fp8_e32 v127, v125
	s_nop 0
	v_sub_f32_e32 v128, v122, v126
	v_sub_f32_e32 v129, v123, v127
	v_cvt_pk_fp8_f32 v124, v128, v128
	v_cvt_pk_fp8_f32 v125, v129, v129
	s_nop 0
	ds_write_b8 v119, v124 offset:4224
	ds_write_b8 v119, v125 offset:4288
	v_cvt_f32_fp8_e32 v126, v124
	v_cvt_f32_fp8_e32 v127, v125
	s_nop 0
	v_sub_f32_e32 v128, v128, v126
	v_sub_f32_e32 v129, v129, v127
	v_cvt_pk_fp8_f32 v124, v128, v128
	v_cvt_pk_fp8_f32 v125, v129, v129
	s_nop 0
	ds_write_b8 v119, v124 offset:4352
	ds_write_b8 v119, v125 offset:4416
	ds_read2st64_b32 v[120:121], v118 offset0:20 offset1:21
	s_waitcnt lgkmcnt(0)
; #define LAS __attribute__((address_space(3)))
; #define XFENCE() asm volatile("" ::: "memory")
; __device__ __forceinline__ void expert_phase(const Frame& F, int l, int xcc, LAS unsigned char* wl, const LAS unsigned char* zb) {
;     ...
;             auto v_rows = [&](int i, URows& R) {
;                 const unsigned char* Vsl = VBl + (size_t)slice_of(i) * XSL_BYTES;
;                 const u32x4 ia = *(const LAS u32x4*)(IDL + (i & 7) * 256 + rr * 32), ib = *(const LAS u32x4*)(IDL + (i & 7) * 256 + rr * 32 + 16);
; #pragma unroll
;                 for (int j = 0; j < 16; ++j) { const unsigned w = j < 8 ? ia[(j >> 1) & 3] : ib[(j >> 1) & 3]; const unsigned e = (j & 1) ? (w >> 16) : (w & 0xffffu);
;                     R.r[j] = ldo_u4(Vsl, e * 128u + 16u * pc); }
;             };
;     ...
;             URows RA, RB;
;             v_rows(0, RA);
;             XFENCE();
; #pragma unroll 1
;             for (int i = 0; i < 64; i += 2) {
;                 const int i2 = i + 2 < 64 ? i + 2 : 63;
;                 v_rows(i + 1, RB);
	v_cvt_f32_f16_e32 v122, v120
	v_cvt_f32_f16_e32 v123, v121
	v_cvt_pk_fp8_f32 v124, v122, v122
	v_cvt_pk_fp8_f32 v125, v123, v123
	s_nop 0
	ds_write_b8 v119, v124 offset:5120
	ds_write_b8 v119, v125 offset:5184
	v_cvt_f32_fp8_e32 v126, v124
	v_cvt_f32_fp8_e32 v127, v125
	s_nop 0
	v_sub_f32_e32 v128, v122, v126
	v_sub_f32_e32 v129, v123, v127
	v_cvt_pk_fp8_f32 v124, v128, v128
	v_cvt_pk_fp8_f32 v125, v129, v129
	s_nop 0
	ds_write_b8 v119, v124 offset:5248
	ds_write_b8 v119, v125 offset:5312
	v_cvt_f32_fp8_e32 v126, v124
	v_cvt_f32_fp8_e32 v127, v125
	s_nop 0
	v_sub_f32_e32 v128, v128, v126
	v_sub_f32_e32 v129, v129, v127
	v_cvt_pk_fp8_f32 v124, v128, v128
	v_cvt_pk_fp8_f32 v125, v129, v129
	s_nop 0
	ds_write_b8 v119, v124 offset:5376
	ds_write_b8 v119, v125 offset:5440
	ds_read2st64_b32 v[120:121], v118 offset0:24 offset1:25
	s_waitcnt lgkmcnt(0)
	v_cvt_f32_f16_e32 v122, v120
	v_cvt_f32_f16_e32 v123, v121
	v_cvt_pk_fp8_f32 v124, v122, v122
	v_cvt_pk_fp8_f32 v125, v123, v123
	s_nop 0
	ds_write_b8 v119, v124 offset:6144
	ds_write_b8 v119, v125 offset:6208
	v_cvt_f32_fp8_e32 v126, v124
	v_cvt_f32_fp8_e32 v127, v125
	s_nop 0
	v_sub_f32_e32 v128, v122, v126
	v_sub_f32_e32 v129, v123, v127
	v_cvt_pk_fp8_f32 v124, v128, v128
	v_cvt_pk_fp8_f32 v125, v129, v129
	s_nop 0
	ds_write_b8 v119, v124 offset:6272
	ds_write_b8 v119, v125 offset:6336
	v_cvt_f32_fp8_e32 v126, v124
	v_cvt_f32_fp8_e32 v127, v125
	s_nop 0
	v_sub_f32_e32 v128, v128, v126
	v_sub_f32_e32 v129, v129, v127
	v_cvt_pk_fp8_f32 v124, v128, v128
	v_cvt_pk_fp8_f32 v125, v129, v129
	s_nop 0
	ds_write_b8 v119, v124 offset:6400
	ds_write_b8 v119, v125 offset:6464
	ds_read2st64_b32 v[120:121], v118 offset0:28 offset1:29
	s_waitcnt lgkmcnt(0)
	v_cvt_f32_f16_e32 v122, v120
	v_cvt_f32_f16_e32 v123, v121
	v_cvt_pk_fp8_f32 v124, v122, v122
	v_cvt_pk_fp8_f32 v125, v123, v123
	s_nop 0
	ds_write_b8 v119, v124 offset:7168
	ds_write_b8 v119, v125 offset:7232
	v_cvt_f32_fp8_e32 v126, v124
	v_cvt_f32_fp8_e32 v127, v125
	s_nop 0
	v_sub_f32_e32 v128, v122, v126
	v_sub_f32_e32 v129, v123, v127
	v_cvt_pk_fp8_f32 v124, v128, v128
	v_cvt_pk_fp8_f32 v125, v129, v129
	s_nop 0
	ds_write_b8 v119, v124 offset:7296
	ds_write_b8 v119, v125 offset:7360
	v_cvt_f32_fp8_e32 v126, v124
	v_cvt_f32_fp8_e32 v127, v125
	s_nop 0
	v_sub_f32_e32 v128, v128, v126
	v_sub_f32_e32 v129, v129, v127
	v_cvt_pk_fp8_f32 v124, v128, v128
	v_cvt_pk_fp8_f32 v125, v129, v129
	s_nop 0
	ds_write_b8 v119, v124 offset:7424
	ds_write_b8 v119, v125 offset:7488
	s_mov_b32 s67, 0
	s_and_b32 s33, s67, 7
	s_lshr_b32 s58, s67, 3
	s_add_i32 s58, s58, s96
	s_and_b32 s58, s58, 7
	s_mul_i32 s8, s33, s82
	s_add_i32 s8, s8, s26
	s_cmpk_lt_i32 s8, 0x4000
	s_cselect_b32 s8, s8, s26
	s_lshl_b32 s78, s58, 21
	s_add_u32 s64, s57, s78
	s_addc_u32 s65, s70, 0
	s_lshl_b32 s78, s33, 8
	v_add_u32_e32 v123, s78, v112
	ds_read_b64 v[108:109], v123 offset:0
	s_waitcnt lgkmcnt(0)
	v_lshlrev_b32_e32 v208, 7, v108
	v_and_or_b32 v208, v208, s77, v113
	global_load_dwordx4 v[0:3], v208, s[64:65]
	v_bfe_u32 v209, v108, 16, 16
	v_lshl_or_b32 v209, v209, 7, v113
	global_load_dwordx4 v[4:7], v209, s[64:65]
	v_lshlrev_b32_e32 v208, 7, v109
	v_and_or_b32 v208, v208, s77, v113
	global_load_dwordx4 v[8:11], v208, s[64:65]
	v_bfe_u32 v209, v109, 16, 16
	v_lshl_or_b32 v209, v209, 7, v113
	global_load_dwordx4 v[12:15], v209, s[64:65]
	s_lshl_b32 s78, s33, 8
	v_add_u32_e32 v123, s78, v112
	ds_read_b64 v[226:227], v123 offset:64
	s_waitcnt lgkmcnt(0)
	v_lshlrev_b32_e32 v208, 7, v226
	v_and_or_b32 v208, v208, s77, v113
	global_load_dwordx4 v[16:19], v208, s[64:65]
	v_bfe_u32 v209, v226, 16, 16
	v_lshl_or_b32 v209, v209, 7, v113
	global_load_dwordx4 v[20:23], v209, s[64:65]
	v_lshlrev_b32_e32 v208, 7, v227
	v_and_or_b32 v208, v208, s77, v113
	global_load_dwordx4 v[24:27], v208, s[64:65]
	v_bfe_u32 v209, v227, 16, 16
	v_lshl_or_b32 v209, v209, 7, v113
	global_load_dwordx4 v[28:31], v209, s[64:65]
	s_lshl_b32 s78, s33, 8
	v_add_u32_e32 v123, s78, v112
	ds_read_b64 v[108:109], v123 offset:128
	s_waitcnt lgkmcnt(0)
	v_lshlrev_b32_e32 v208, 7, v108
	v_and_or_b32 v208, v208, s77, v113
	global_load_dwordx4 v[32:35], v208, s[64:65]
	v_bfe_u32 v209, v108, 16, 16
	v_lshl_or_b32 v209, v209, 7, v113
	global_load_dwordx4 v[36:39], v209, s[64:65]
	v_lshlrev_b32_e32 v208, 7, v109
	v_and_or_b32 v208, v208, s77, v113
	global_load_dwordx4 v[40:43], v208, s[64:65]
	v_bfe_u32 v209, v109, 16, 16
	v_lshl_or_b32 v209, v209, 7, v113
	global_load_dwordx4 v[44:47], v209, s[64:65]
	s_lshl_b32 s78, s33, 8
	v_add_u32_e32 v123, s78, v112
	ds_read_b64 v[226:227], v123 offset:192
	s_waitcnt lgkmcnt(0)
	v_lshlrev_b32_e32 v208, 7, v226
	v_and_or_b32 v208, v208, s77, v113
	global_load_dwordx4 v[48:51], v208, s[64:65]
	v_bfe_u32 v209, v226, 16, 16
	v_lshl_or_b32 v209, v209, 7, v113
	global_load_dwordx4 v[52:55], v209, s[64:65]
	v_lshlrev_b32_e32 v208, 7, v227
	v_and_or_b32 v208, v208, s77, v113
	global_load_dwordx4 v[56:59], v208, s[64:65]
	v_bfe_u32 v209, v227, 16, 16
	v_lshl_or_b32 v209, v209, 7, v113
	global_load_dwordx4 v[60:63], v209, s[64:65]
	s_ashr_i32 s55, s8, 31
	s_mov_b32 s54, s8
	s_lshl_b64 s[54:55], s[54:55], 12
	s_add_u32 s54, s90, s54
	s_addc_u32 s55, s91, s55
	s_lshl_b32 s78, s58, 9
	s_add_u32 s54, s54, s78
	s_addc_u32 s55, s55, 0
	v_lshl_add_u64 v[208:209], s[54:55], 0, v[184:185]
	global_load_dwordx2 v[172:173], v[208:209], off
	s_mov_b32 s4, 1
	s_and_b32 s33, s4, 7
	s_lshr_b32 s58, s4, 3
	s_add_i32 s58, s58, s96
	s_and_b32 s58, s58, 7
	s_mul_i32 s9, s33, s82
	s_add_i32 s9, s9, s26
	s_cmpk_lt_i32 s9, 0x4000
	s_cselect_b32 s9, s9, s26
	s_mov_b32 s2, 0
	s_waitcnt vmcnt(12)
	ds_write_b128 v110, v[0:3] offset:0
	ds_write_b128 v110, v[4:7] offset:144
	ds_write_b128 v110, v[8:11] offset:288
	ds_write_b128 v110, v[12:15] offset:432
	s_lshl_b32 s78, s2, 10
	v_add_u32_e32 v120, s78, v114
	v_mov_b32_e32 v121, 0x1a000
	v_cndmask_b32_e64 v122, v121, v120, s[30:31]
	v_cndmask_b32_e64 v121, v121, v120, s[44:45]
	ds_read_b128 v[80:83], v122
	ds_read_b128 v[84:87], v121
	s_lshl_b32 s78, s33, 8
	v_add_u32_e32 v123, s78, v112
	ds_read_b64 v[108:109], v123 offset:0
	ds_read_b64_tr_b4 v[64:65], v111 offset:0
	ds_read_b64_tr_b4 v[66:67], v111 offset:2304
	ds_read_b64_tr_b4 v[68:69], v111 offset:32
	ds_read_b64_tr_b4 v[70:71], v111 offset:2336
	ds_read_b64_tr_b4 v[72:73], v111 offset:64
	ds_read_b64_tr_b4 v[74:75], v111 offset:2368
	ds_read_b64_tr_b4 v[76:77], v111 offset:96
	ds_read_b64_tr_b4 v[78:79], v111 offset:2400
	s_nop 0
	s_nop 0
